# attention inner loops: packed v_pk_mul_f32 accumulator rescales split into scalar v_mul_f32 pairs (docs 7.5), bit-identical
# baseline (speedup 1.0000x reference)
.LBB0_258:
	v_subrev_u32_e32 v138, s15, v188
	v_add_u32_e32 v138, 64, v138
	v_cvt_f32_i32_e32 v138, v138
	v_mul_f32_e64 v147, -v157, v138
	v_fma_f32 v153, -v157, v138, v157
	v_fma_f32 v194, 0, v157, v147
	v_fmac_f32_e32 v153, 0x3e38aa3b, v51
	v_fma_f32 v195, 2.0, v157, v147
	v_fmac_f32_e32 v194, 0x3e38aa3b, v50
	v_fmamk_f32 v196, v157, 0x40400000, v147
	v_max3_f32 v138, v194, s81, v153
	v_fmac_f32_e32 v195, 0x3e38aa3b, v52
	v_fmac_f32_e32 v196, 0x3e38aa3b, v53
	v_fmamk_f32 v197, v157, 0x41000000, v147
	v_fmamk_f32 v198, v157, 0x41100000, v147
	v_max3_f32 v138, v138, v195, v196
	v_fmac_f32_e32 v197, 0x3e38aa3b, v54
	v_fmac_f32_e32 v198, 0x3e38aa3b, v55
	v_fmamk_f32 v199, v157, 0x41200000, v147
	v_fmamk_f32 v200, v157, 0x41300000, v147
	v_max3_f32 v138, v138, v197, v198
	v_fmac_f32_e32 v199, 0x3e38aa3b, v56
	v_fmac_f32_e32 v200, 0x3e38aa3b, v57
	v_fmamk_f32 v201, v157, 0x41800000, v147
	v_fmamk_f32 v202, v157, 0x41880000, v147
	v_max3_f32 v138, v138, v199, v200
	v_fmac_f32_e32 v201, 0x3e38aa3b, v58
	v_fmac_f32_e32 v202, 0x3e38aa3b, v59
	v_fmamk_f32 v203, v157, 0x41900000, v147
	v_fmamk_f32 v204, v157, 0x41980000, v147
	v_max3_f32 v138, v138, v201, v202
	v_fmac_f32_e32 v203, 0x3e38aa3b, v60
	v_fmac_f32_e32 v204, 0x3e38aa3b, v61
	v_fmamk_f32 v205, v157, 0x41c00000, v147
	v_fmamk_f32 v206, v157, 0x41c80000, v147
	v_max3_f32 v138, v138, v203, v204
	v_fmac_f32_e32 v205, 0x3e38aa3b, v62
	v_fmac_f32_e32 v206, 0x3e38aa3b, v63
	v_fmamk_f32 v207, v157, 0x41d00000, v147
	v_fmac_f32_e32 v147, 0x41d80000, v157
	v_max3_f32 v138, v138, v205, v206
	v_fmac_f32_e32 v207, 0x3e38aa3b, v64
	v_fmac_f32_e32 v147, 0x3e38aa3b, v65
	v_max3_f32 v142, v138, v207, v147
	ds_bpermute_b32 v143, v161, v142
	ds_read2_b64 v[138:141], v176 offset1:2
	s_waitcnt lgkmcnt(1)
	v_max3_f32 v208, v189, v142, v143
	v_sub_f32_e32 v142, v189, v208
	v_sub_f32_e32 v189, v194, v208
	v_sub_f32_e32 v194, v195, v208
	v_exp_f32_e32 v152, v142
	v_exp_f32_e32 v209, v194
	v_sub_f32_e32 v194, v196, v208
	v_exp_f32_e32 v210, v194
	v_sub_f32_e32 v194, v197, v208
	v_exp_f32_e32 v211, v194
	v_sub_f32_e32 v194, v198, v208
	v_exp_f32_e32 v198, v194
	v_sub_f32_e32 v194, v199, v208
	v_mul_f32_e32 v48, v152, v48
	v_mul_f32_e32 v49, v152, v49
	v_mul_f32_e32 v46, v152, v46
	v_mul_f32_e32 v47, v152, v47
	v_mul_f32_e32 v44, v152, v44
	v_mul_f32_e32 v45, v152, v45
	v_mul_f32_e32 v42, v152, v42
	v_mul_f32_e32 v43, v152, v43
	v_mul_f32_e32 v40, v152, v40
	v_mul_f32_e32 v41, v152, v41
	v_mul_f32_e32 v38, v152, v38
	v_mul_f32_e32 v39, v152, v39
	v_mul_f32_e32 v36, v152, v36
	v_mul_f32_e32 v37, v152, v37
	v_mul_f32_e32 v34, v152, v34
	v_mul_f32_e32 v35, v152, v35
	v_mul_f32_e32 v32, v152, v32
	v_mul_f32_e32 v33, v152, v33
	v_mul_f32_e32 v30, v152, v30
	v_mul_f32_e32 v31, v152, v31
	v_mul_f32_e32 v28, v152, v28
	v_mul_f32_e32 v29, v152, v29
	v_mul_f32_e32 v26, v152, v26
	v_mul_f32_e32 v27, v152, v27
	v_mul_f32_e32 v24, v152, v24
	v_mul_f32_e32 v25, v152, v25
	v_mul_f32_e32 v22, v152, v22
	v_mul_f32_e32 v23, v152, v23
	v_mul_f32_e32 v20, v152, v20
	v_mul_f32_e32 v21, v152, v21
	v_mul_f32_e32 v18, v152, v18
	v_mul_f32_e32 v19, v152, v19
	v_sub_f32_e32 v153, v153, v208
	v_exp_f32_e32 v199, v194
	v_sub_f32_e32 v194, v200, v208
	v_exp_f32_e32 v189, v189
	v_exp_f32_e32 v153, v153
	v_exp_f32_e32 v200, v194
	v_cvt_pk_bf16_f32 v195, v209, v210
	v_cvt_pk_bf16_f32 v196, v211, v198
	v_cvt_pk_bf16_f32 v194, v189, v153
	v_cvt_pk_bf16_f32 v197, v199, v200
	v_add_f32_e32 v189, 0, v189
	ds_read2_b64 v[142:145], v177 offset1:2
	ds_read2_b64 v[148:151], v178 offset1:2
	ds_read2_b64 v[190:193], v179 offset1:2
	s_waitcnt lgkmcnt(3)
	v_mfma_f32_32x32x16_bf16 v[34:49], v[138:141], v[194:197], v[34:49]
	v_add_f32_e32 v138, v153, v189
	v_add_f32_e32 v138, v209, v138
	v_add_f32_e32 v138, v210, v138
	v_add_f32_e32 v138, v211, v138
	v_add_f32_e32 v138, v198, v138
	v_add_f32_e32 v138, v199, v138
	v_add_f32_e32 v153, v200, v138
	v_sub_f32_e32 v138, v201, v208
	s_waitcnt lgkmcnt(1)
	v_mfma_f32_32x32x16_bf16 v[18:33], v[148:151], v[194:197], v[18:33]
	v_exp_f32_e32 v148, v138
	v_sub_f32_e32 v138, v202, v208
	v_exp_f32_e32 v149, v138
	v_sub_f32_e32 v138, v203, v208
	v_exp_f32_e32 v150, v138
	v_sub_f32_e32 v138, v204, v208
	v_exp_f32_e32 v151, v138
	v_sub_f32_e32 v138, v205, v208
	v_exp_f32_e32 v189, v138
	v_sub_f32_e32 v138, v206, v208
	v_exp_f32_e32 v194, v138
	v_sub_f32_e32 v138, v207, v208
	v_exp_f32_e32 v195, v138
	v_sub_f32_e32 v138, v147, v208
	v_exp_f32_e32 v147, v138
	v_cvt_pk_bf16_f32 v138, v148, v149
	v_cvt_pk_bf16_f32 v139, v150, v151
	v_cvt_pk_bf16_f32 v140, v189, v194
	v_cvt_pk_bf16_f32 v141, v195, v147
	v_add_f32_e32 v148, v148, v153
	s_nop 0
	v_mfma_f32_32x32x16_bf16 v[34:49], v[142:145], v[138:141], v[34:49]
	v_add_f32_e32 v142, v149, v148
	v_add_f32_e32 v142, v150, v142
	v_add_f32_e32 v142, v151, v142
	v_add_f32_e32 v142, v189, v142
	v_add_f32_e32 v142, v194, v142
	v_add_f32_e32 v142, v195, v142
	v_add_f32_e32 v142, v147, v142
	s_waitcnt lgkmcnt(0)
	v_mfma_f32_32x32x16_bf16 v[18:33], v[190:193], v[138:141], v[18:33]
	v_fmac_f32_e32 v142, v146, v152
	v_mov_b32_e32 v189, v208
	v_mov_b32_e32 v146, v142
	s_cmp_gt_i32 s17, 1
	s_cbranch_scc0 .LBB0_265

.LBB0_263:
	v_subrev_u32_e32 v138, s15, v188
	v_add_u32_e32 v138, 32, v138
	v_cvt_f32_i32_e32 v138, v138
	v_mul_f32_e64 v147, -v157, v138
	v_fma_f32 v153, -v157, v138, v157
	v_fma_f32 v194, 0, v157, v147
	v_fmac_f32_e32 v153, 0x3e38aa3b, v3
	v_fma_f32 v195, 2.0, v157, v147
	v_fmac_f32_e32 v194, 0x3e38aa3b, v2
	v_fmamk_f32 v196, v157, 0x40400000, v147
	v_max3_f32 v138, v194, s81, v153
	v_fmac_f32_e32 v195, 0x3e38aa3b, v4
	v_fmac_f32_e32 v196, 0x3e38aa3b, v5
	v_fmamk_f32 v197, v157, 0x41000000, v147
	v_fmamk_f32 v198, v157, 0x41100000, v147
	v_max3_f32 v138, v138, v195, v196
	v_fmac_f32_e32 v197, 0x3e38aa3b, v6
	v_fmac_f32_e32 v198, 0x3e38aa3b, v7
	v_fmamk_f32 v199, v157, 0x41200000, v147
	v_fmamk_f32 v200, v157, 0x41300000, v147
	v_max3_f32 v138, v138, v197, v198
	v_fmac_f32_e32 v199, 0x3e38aa3b, v8
	v_fmac_f32_e32 v200, 0x3e38aa3b, v9
	v_fmamk_f32 v201, v157, 0x41800000, v147
	v_fmamk_f32 v202, v157, 0x41880000, v147
	v_max3_f32 v138, v138, v199, v200
	v_fmac_f32_e32 v201, 0x3e38aa3b, v10
	v_fmac_f32_e32 v202, 0x3e38aa3b, v11
	v_fmamk_f32 v203, v157, 0x41900000, v147
	v_fmamk_f32 v204, v157, 0x41980000, v147
	v_max3_f32 v138, v138, v201, v202
	v_fmac_f32_e32 v203, 0x3e38aa3b, v12
	v_fmac_f32_e32 v204, 0x3e38aa3b, v13
	v_fmamk_f32 v205, v157, 0x41c00000, v147
	v_fmamk_f32 v206, v157, 0x41c80000, v147
	v_max3_f32 v138, v138, v203, v204
	v_fmac_f32_e32 v205, 0x3e38aa3b, v14
	v_fmac_f32_e32 v206, 0x3e38aa3b, v15
	v_fmamk_f32 v207, v157, 0x41d00000, v147
	v_fmac_f32_e32 v147, 0x41d80000, v157
	v_max3_f32 v138, v138, v205, v206
	v_fmac_f32_e32 v207, 0x3e38aa3b, v16
	v_fmac_f32_e32 v147, 0x3e38aa3b, v17
	v_max3_f32 v142, v138, v207, v147
	ds_bpermute_b32 v143, v161, v142
	ds_read2_b64 v[138:141], v172 offset1:2
	s_waitcnt lgkmcnt(1)
	v_max3_f32 v208, v189, v142, v143
	v_sub_f32_e32 v142, v189, v208
	v_sub_f32_e32 v189, v194, v208
	v_sub_f32_e32 v194, v195, v208
	v_exp_f32_e32 v152, v142
	v_exp_f32_e32 v209, v194
	v_sub_f32_e32 v194, v196, v208
	v_exp_f32_e32 v210, v194
	v_sub_f32_e32 v194, v197, v208
	v_exp_f32_e32 v211, v194
	v_sub_f32_e32 v194, v198, v208
	v_exp_f32_e32 v198, v194
	v_sub_f32_e32 v194, v199, v208
	v_mul_f32_e32 v48, v152, v48
	v_mul_f32_e32 v49, v152, v49
	v_mul_f32_e32 v46, v152, v46
	v_mul_f32_e32 v47, v152, v47
	v_mul_f32_e32 v44, v152, v44
	v_mul_f32_e32 v45, v152, v45
	v_mul_f32_e32 v42, v152, v42
	v_mul_f32_e32 v43, v152, v43
	v_mul_f32_e32 v40, v152, v40
	v_mul_f32_e32 v41, v152, v41
	v_mul_f32_e32 v38, v152, v38
	v_mul_f32_e32 v39, v152, v39
	v_mul_f32_e32 v36, v152, v36
	v_mul_f32_e32 v37, v152, v37
	v_mul_f32_e32 v34, v152, v34
	v_mul_f32_e32 v35, v152, v35
	v_mul_f32_e32 v32, v152, v32
	v_mul_f32_e32 v33, v152, v33
	v_mul_f32_e32 v30, v152, v30
	v_mul_f32_e32 v31, v152, v31
	v_mul_f32_e32 v28, v152, v28
	v_mul_f32_e32 v29, v152, v29
	v_mul_f32_e32 v26, v152, v26
	v_mul_f32_e32 v27, v152, v27
	v_mul_f32_e32 v24, v152, v24
	v_mul_f32_e32 v25, v152, v25
	v_mul_f32_e32 v22, v152, v22
	v_mul_f32_e32 v23, v152, v23
	v_mul_f32_e32 v20, v152, v20
	v_mul_f32_e32 v21, v152, v21
	v_mul_f32_e32 v18, v152, v18
	v_mul_f32_e32 v19, v152, v19
	v_sub_f32_e32 v153, v153, v208
	v_exp_f32_e32 v199, v194
	v_sub_f32_e32 v194, v200, v208
	v_exp_f32_e32 v189, v189
	v_exp_f32_e32 v153, v153
	v_exp_f32_e32 v200, v194
	v_cvt_pk_bf16_f32 v195, v209, v210
	v_cvt_pk_bf16_f32 v196, v211, v198
	v_cvt_pk_bf16_f32 v194, v189, v153
	v_cvt_pk_bf16_f32 v197, v199, v200
	v_add_f32_e32 v189, 0, v189
	ds_read2_b64 v[142:145], v173 offset1:2
	ds_read2_b64 v[148:151], v174 offset1:2
	ds_read2_b64 v[190:193], v175 offset1:2
	s_waitcnt lgkmcnt(3)
	v_mfma_f32_32x32x16_bf16 v[34:49], v[138:141], v[194:197], v[34:49]
	v_add_f32_e32 v138, v153, v189
	v_add_f32_e32 v138, v209, v138
	v_add_f32_e32 v138, v210, v138
	v_add_f32_e32 v138, v211, v138
	v_add_f32_e32 v138, v198, v138
	v_add_f32_e32 v138, v199, v138
	v_add_f32_e32 v153, v200, v138
	v_sub_f32_e32 v138, v201, v208
	s_waitcnt lgkmcnt(1)
	v_mfma_f32_32x32x16_bf16 v[18:33], v[148:151], v[194:197], v[18:33]
	v_exp_f32_e32 v148, v138
	v_sub_f32_e32 v138, v202, v208
	v_exp_f32_e32 v149, v138
	v_sub_f32_e32 v138, v203, v208
	v_exp_f32_e32 v150, v138
	v_sub_f32_e32 v138, v204, v208
	v_exp_f32_e32 v151, v138
	v_sub_f32_e32 v138, v205, v208
	v_exp_f32_e32 v189, v138
	v_sub_f32_e32 v138, v206, v208
	v_exp_f32_e32 v194, v138
	v_sub_f32_e32 v138, v207, v208
	v_exp_f32_e32 v195, v138
	v_sub_f32_e32 v138, v147, v208
	v_exp_f32_e32 v147, v138
	v_cvt_pk_bf16_f32 v138, v148, v149
	v_cvt_pk_bf16_f32 v139, v150, v151
	v_cvt_pk_bf16_f32 v140, v189, v194
	v_cvt_pk_bf16_f32 v141, v195, v147
	v_add_f32_e32 v148, v148, v153
	s_nop 0
	v_mfma_f32_32x32x16_bf16 v[34:49], v[142:145], v[138:141], v[34:49]
	v_add_f32_e32 v142, v149, v148
	v_add_f32_e32 v142, v150, v142
	v_add_f32_e32 v142, v151, v142
	v_add_f32_e32 v142, v189, v142
	v_add_f32_e32 v142, v194, v142
	v_add_f32_e32 v142, v195, v142
	v_add_f32_e32 v142, v147, v142
	s_waitcnt lgkmcnt(0)
	v_mfma_f32_32x32x16_bf16 v[18:33], v[190:193], v[138:141], v[18:33]
	v_fmac_f32_e32 v142, v146, v152
	v_mov_b32_e32 v189, v208
	v_mov_b32_e32 v146, v142
	s_cmp_gt_i32 s17, 2
	s_cbranch_scc0 .LBB0_256

.LBB0_267:
	v_subrev_u32_e32 v138, s15, v188
	v_add_u32_e32 v138, 0x60, v138
	v_cvt_f32_i32_e32 v138, v138
	v_mul_f32_e64 v147, -v157, v138
	v_fma_f32 v153, -v157, v138, v157
	v_fma_f32 v194, 0, v157, v147
	v_fmac_f32_e32 v153, 0x3e38aa3b, v3
	v_fma_f32 v195, 2.0, v157, v147
	v_fmac_f32_e32 v194, 0x3e38aa3b, v2
	v_fmamk_f32 v196, v157, 0x40400000, v147
	v_max3_f32 v138, v194, s81, v153
	v_fmac_f32_e32 v195, 0x3e38aa3b, v4
	v_fmac_f32_e32 v196, 0x3e38aa3b, v5
	v_fmamk_f32 v197, v157, 0x41000000, v147
	v_fmamk_f32 v198, v157, 0x41100000, v147
	v_max3_f32 v138, v138, v195, v196
	v_fmac_f32_e32 v197, 0x3e38aa3b, v6
	v_fmac_f32_e32 v198, 0x3e38aa3b, v7
	v_fmamk_f32 v199, v157, 0x41200000, v147
	v_fmamk_f32 v200, v157, 0x41300000, v147
	v_max3_f32 v138, v138, v197, v198
	v_fmac_f32_e32 v199, 0x3e38aa3b, v8
	v_fmac_f32_e32 v200, 0x3e38aa3b, v9
	v_fmamk_f32 v201, v157, 0x41800000, v147
	v_fmamk_f32 v202, v157, 0x41880000, v147
	v_max3_f32 v138, v138, v199, v200
	v_fmac_f32_e32 v201, 0x3e38aa3b, v10
	v_fmac_f32_e32 v202, 0x3e38aa3b, v11
	v_fmamk_f32 v203, v157, 0x41900000, v147
	v_fmamk_f32 v204, v157, 0x41980000, v147
	v_max3_f32 v138, v138, v201, v202
	v_fmac_f32_e32 v203, 0x3e38aa3b, v12
	v_fmac_f32_e32 v204, 0x3e38aa3b, v13
	v_fmamk_f32 v205, v157, 0x41c00000, v147
	v_fmamk_f32 v206, v157, 0x41c80000, v147
	v_max3_f32 v138, v138, v203, v204
	v_fmac_f32_e32 v205, 0x3e38aa3b, v14
	v_fmac_f32_e32 v206, 0x3e38aa3b, v15
	v_fmamk_f32 v207, v157, 0x41d00000, v147
	v_fmac_f32_e32 v147, 0x41d80000, v157
	v_max3_f32 v138, v138, v205, v206
	v_fmac_f32_e32 v207, 0x3e38aa3b, v16
	v_fmac_f32_e32 v147, 0x3e38aa3b, v17
	v_max3_f32 v142, v138, v207, v147
	ds_bpermute_b32 v143, v161, v142
	ds_read2_b64 v[138:141], v180 offset1:2
	s_waitcnt lgkmcnt(1)
	v_max3_f32 v208, v189, v142, v143
	v_sub_f32_e32 v142, v189, v208
	v_sub_f32_e32 v189, v194, v208
	v_sub_f32_e32 v194, v195, v208
	v_exp_f32_e32 v152, v142
	v_exp_f32_e32 v209, v194
	v_sub_f32_e32 v194, v196, v208
	v_exp_f32_e32 v210, v194
	v_sub_f32_e32 v194, v197, v208
	v_exp_f32_e32 v211, v194
	v_sub_f32_e32 v194, v198, v208
	v_exp_f32_e32 v198, v194
	v_sub_f32_e32 v194, v199, v208
	v_mul_f32_e32 v48, v152, v48
	v_mul_f32_e32 v49, v152, v49
	v_mul_f32_e32 v46, v152, v46
	v_mul_f32_e32 v47, v152, v47
	v_mul_f32_e32 v44, v152, v44
	v_mul_f32_e32 v45, v152, v45
	v_mul_f32_e32 v42, v152, v42
	v_mul_f32_e32 v43, v152, v43
	v_mul_f32_e32 v40, v152, v40
	v_mul_f32_e32 v41, v152, v41
	v_mul_f32_e32 v38, v152, v38
	v_mul_f32_e32 v39, v152, v39
	v_mul_f32_e32 v36, v152, v36
	v_mul_f32_e32 v37, v152, v37
	v_mul_f32_e32 v34, v152, v34
	v_mul_f32_e32 v35, v152, v35
	v_mul_f32_e32 v32, v152, v32
	v_mul_f32_e32 v33, v152, v33
	v_mul_f32_e32 v30, v152, v30
	v_mul_f32_e32 v31, v152, v31
	v_mul_f32_e32 v28, v152, v28
	v_mul_f32_e32 v29, v152, v29
	v_mul_f32_e32 v26, v152, v26
	v_mul_f32_e32 v27, v152, v27
	v_mul_f32_e32 v24, v152, v24
	v_mul_f32_e32 v25, v152, v25
	v_mul_f32_e32 v22, v152, v22
	v_mul_f32_e32 v23, v152, v23
	v_mul_f32_e32 v20, v152, v20
	v_mul_f32_e32 v21, v152, v21
	v_mul_f32_e32 v18, v152, v18
	v_mul_f32_e32 v19, v152, v19
	v_sub_f32_e32 v153, v153, v208
	v_exp_f32_e32 v199, v194
	v_sub_f32_e32 v194, v200, v208
	v_exp_f32_e32 v189, v189
	v_exp_f32_e32 v153, v153
	v_exp_f32_e32 v200, v194
	v_cvt_pk_bf16_f32 v195, v209, v210
	v_cvt_pk_bf16_f32 v196, v211, v198
	v_cvt_pk_bf16_f32 v194, v189, v153
	v_cvt_pk_bf16_f32 v197, v199, v200
	v_add_f32_e32 v189, 0, v189
	ds_read2_b64 v[142:145], v181 offset1:2
	ds_read2_b64 v[148:151], v182 offset1:2
	ds_read2_b64 v[190:193], v183 offset1:2
	s_waitcnt lgkmcnt(3)
	v_mfma_f32_32x32x16_bf16 v[34:49], v[138:141], v[194:197], v[34:49]
	v_add_f32_e32 v138, v153, v189
	v_add_f32_e32 v138, v209, v138
	v_add_f32_e32 v138, v210, v138
	v_add_f32_e32 v138, v211, v138
	v_add_f32_e32 v138, v198, v138
	v_add_f32_e32 v138, v199, v138
	v_add_f32_e32 v153, v200, v138
	v_sub_f32_e32 v138, v201, v208
	s_waitcnt lgkmcnt(1)
	v_mfma_f32_32x32x16_bf16 v[18:33], v[148:151], v[194:197], v[18:33]
	v_exp_f32_e32 v148, v138
	v_sub_f32_e32 v138, v202, v208
	v_exp_f32_e32 v149, v138
	v_sub_f32_e32 v138, v203, v208
	v_exp_f32_e32 v150, v138
	v_sub_f32_e32 v138, v204, v208
	v_exp_f32_e32 v151, v138
	v_sub_f32_e32 v138, v205, v208
	v_exp_f32_e32 v189, v138
	v_sub_f32_e32 v138, v206, v208
	v_exp_f32_e32 v194, v138
	v_sub_f32_e32 v138, v207, v208
	v_exp_f32_e32 v195, v138
	v_sub_f32_e32 v138, v147, v208
	v_exp_f32_e32 v147, v138
	v_cvt_pk_bf16_f32 v138, v148, v149
	v_cvt_pk_bf16_f32 v139, v150, v151
	v_cvt_pk_bf16_f32 v140, v189, v194
	v_cvt_pk_bf16_f32 v141, v195, v147
	v_add_f32_e32 v148, v148, v153
	s_nop 0
	v_mfma_f32_32x32x16_bf16 v[34:49], v[142:145], v[138:141], v[34:49]
	v_add_f32_e32 v142, v149, v148
	v_add_f32_e32 v142, v150, v142
	v_add_f32_e32 v142, v151, v142
	v_add_f32_e32 v142, v189, v142
	v_add_f32_e32 v142, v194, v142
	v_add_f32_e32 v142, v195, v142
	v_add_f32_e32 v142, v147, v142
	s_waitcnt lgkmcnt(0)
	v_mfma_f32_32x32x16_bf16 v[18:33], v[190:193], v[138:141], v[18:33]
	v_fmac_f32_e32 v142, v146, v152
	v_mov_b32_e32 v189, v208
	v_mov_b32_e32 v146, v142
	s_cmp_gt_i32 s17, 0
	s_cbranch_scc1 .LBB0_271

.LBB0_270:
	v_subrev_u32_e32 v122, s15, v188
	v_add_u32_e32 v123, 0x80, v122
	v_cvt_f32_i32_e32 v124, v123
	s_movk_i32 s15, 0x81
	v_cmp_gt_u32_e32 vcc, s15, v123
	s_movk_i32 s15, 0xff7e
	v_mul_f32_e64 v125, -v157, v124
	v_fma_f32 v124, -v157, v124, v157
	v_fma_f32 v126, 0, v157, v125
	v_fmac_f32_e32 v124, 0x3e38aa3b, v51
	v_fmac_f32_e32 v126, 0x3e38aa3b, v50
	v_add_u32_e32 v50, -2, v122
	v_fma_f32 v51, 2.0, v157, v125
	v_cndmask_b32_e32 v123, v225, v126, vcc
	v_cmp_lt_u32_e32 vcc, s15, v50
	v_fmac_f32_e32 v51, 0x3e38aa3b, v52
	v_add_u32_e32 v52, -3, v122
	v_cndmask_b32_e32 v124, v225, v124, vcc
	v_cmp_lt_u32_e32 vcc, s15, v52
	v_add_u32_e32 v52, -4, v122
	v_max3_f32 v50, v123, s81, v124
	v_cndmask_b32_e32 v127, v225, v51, vcc
	v_fmamk_f32 v51, v157, 0x40400000, v125
	v_fmac_f32_e32 v51, 0x3e38aa3b, v53
	v_cmp_lt_u32_e32 vcc, s15, v52
	v_add_u32_e32 v52, -9, v122
	s_nop 0
	v_cndmask_b32_e32 v128, v225, v51, vcc
	v_fmamk_f32 v51, v157, 0x41000000, v125
	v_fmac_f32_e32 v51, 0x3e38aa3b, v54
	v_cmp_lt_u32_e32 vcc, s15, v52
	v_add_u32_e32 v52, -10, v122
	v_max3_f32 v50, v50, v127, v128
	v_cndmask_b32_e32 v129, v225, v51, vcc
	v_fmamk_f32 v51, v157, 0x41100000, v125
	v_fmac_f32_e32 v51, 0x3e38aa3b, v55
	v_cmp_lt_u32_e32 vcc, s15, v52
	v_add_u32_e32 v52, -11, v122
	s_nop 0
	v_cndmask_b32_e32 v130, v225, v51, vcc
	v_fmamk_f32 v51, v157, 0x41200000, v125
	v_fmac_f32_e32 v51, 0x3e38aa3b, v56
	v_cmp_lt_u32_e32 vcc, s15, v52
	v_add_u32_e32 v52, -12, v122
	v_max3_f32 v50, v50, v129, v130
	v_cndmask_b32_e32 v131, v225, v51, vcc
	v_fmamk_f32 v51, v157, 0x41300000, v125
	v_fmac_f32_e32 v51, 0x3e38aa3b, v57
	v_cmp_lt_u32_e32 vcc, s15, v52
	v_subrev_u32_e32 v52, 17, v122
	s_nop 0
	v_cndmask_b32_e32 v132, v225, v51, vcc
	v_fmamk_f32 v51, v157, 0x41800000, v125
	v_fmac_f32_e32 v51, 0x3e38aa3b, v58
	v_cmp_lt_u32_e32 vcc, s15, v52
	v_subrev_u32_e32 v52, 18, v122
	v_max3_f32 v50, v50, v131, v132
	v_cndmask_b32_e32 v133, v225, v51, vcc
	v_fmamk_f32 v51, v157, 0x41880000, v125
	v_fmac_f32_e32 v51, 0x3e38aa3b, v59
	v_cmp_lt_u32_e32 vcc, s15, v52
	v_subrev_u32_e32 v52, 19, v122
	s_nop 0
	v_cndmask_b32_e32 v134, v225, v51, vcc
	v_fmamk_f32 v51, v157, 0x41900000, v125
	v_fmac_f32_e32 v51, 0x3e38aa3b, v60
	v_cmp_lt_u32_e32 vcc, s15, v52
	v_subrev_u32_e32 v52, 20, v122
	v_max3_f32 v50, v50, v133, v134
	v_cndmask_b32_e32 v135, v225, v51, vcc
	v_fmamk_f32 v51, v157, 0x41980000, v125
	v_fmac_f32_e32 v51, 0x3e38aa3b, v61
	v_cmp_lt_u32_e32 vcc, s15, v52
	v_subrev_u32_e32 v52, 25, v122
	s_nop 0
	v_cndmask_b32_e32 v136, v225, v51, vcc
	v_fmamk_f32 v51, v157, 0x41c00000, v125
	v_fmac_f32_e32 v51, 0x3e38aa3b, v62
	v_cmp_lt_u32_e32 vcc, s15, v52
	v_subrev_u32_e32 v52, 26, v122
	v_max3_f32 v50, v50, v135, v136
	v_cndmask_b32_e32 v137, v225, v51, vcc
	v_fmamk_f32 v51, v157, 0x41c80000, v125
	v_fmac_f32_e32 v51, 0x3e38aa3b, v63
	v_cmp_lt_u32_e32 vcc, s15, v52
	v_subrev_u32_e32 v52, 27, v122
	s_nop 0
	v_cndmask_b32_e32 v138, v225, v51, vcc
	v_fmamk_f32 v51, v157, 0x41d00000, v125
	v_fmac_f32_e32 v51, 0x3e38aa3b, v64
	v_cmp_lt_u32_e32 vcc, s15, v52
	v_fmac_f32_e32 v125, 0x41d80000, v157
	v_fmac_f32_e32 v125, 0x3e38aa3b, v65
	v_cndmask_b32_e32 v139, v225, v51, vcc
	v_subrev_u32_e32 v51, 28, v122
	v_cmp_lt_u32_e32 vcc, s15, v51
	v_max3_f32 v50, v50, v137, v138
	s_nop 0
	v_cndmask_b32_e32 v140, v225, v125, vcc
	v_max3_f32 v54, v50, v139, v140
	ds_bpermute_b32 v55, v161, v54
	ds_read2_b64 v[50:53], v184 offset1:2
	s_waitcnt lgkmcnt(1)
	v_max3_f32 v141, v189, v54, v55
	v_sub_f32_e32 v54, v189, v141
	v_exp_f32_e32 v126, v54
	v_sub_f32_e32 v122, v123, v141
	v_exp_f32_e32 v142, v122
	v_sub_f32_e32 v122, v124, v141
	v_exp_f32_e32 v143, v122
	v_sub_f32_e32 v122, v127, v141
	v_mul_f32_e32 v48, v126, v48
	v_mul_f32_e32 v49, v126, v49
	v_mul_f32_e32 v46, v126, v46
	v_mul_f32_e32 v47, v126, v47
	v_mul_f32_e32 v44, v126, v44
	v_mul_f32_e32 v45, v126, v45
	v_mul_f32_e32 v42, v126, v42
	v_mul_f32_e32 v43, v126, v43
	v_mul_f32_e32 v40, v126, v40
	v_mul_f32_e32 v41, v126, v41
	v_mul_f32_e32 v38, v126, v38
	v_mul_f32_e32 v39, v126, v39
	v_mul_f32_e32 v36, v126, v36
	v_mul_f32_e32 v37, v126, v37
	v_mul_f32_e32 v34, v126, v34
	v_mul_f32_e32 v35, v126, v35
	v_mul_f32_e32 v32, v126, v32
	v_mul_f32_e32 v33, v126, v33
	v_mul_f32_e32 v30, v126, v30
	v_mul_f32_e32 v31, v126, v31
	v_mul_f32_e32 v28, v126, v28
	v_mul_f32_e32 v29, v126, v29
	v_mul_f32_e32 v26, v126, v26
	v_mul_f32_e32 v27, v126, v27
	v_mul_f32_e32 v24, v126, v24
	v_mul_f32_e32 v25, v126, v25
	v_mul_f32_e32 v22, v126, v22
	v_mul_f32_e32 v23, v126, v23
	v_mul_f32_e32 v20, v126, v20
	v_mul_f32_e32 v21, v126, v21
	v_mul_f32_e32 v18, v126, v18
	v_mul_f32_e32 v19, v126, v19
	v_exp_f32_e32 v127, v122
	v_sub_f32_e32 v122, v128, v141
	v_exp_f32_e32 v128, v122
	v_sub_f32_e32 v122, v129, v141
	v_exp_f32_e32 v129, v122
	v_sub_f32_e32 v122, v130, v141
	v_exp_f32_e32 v130, v122
	v_sub_f32_e32 v122, v131, v141
	v_exp_f32_e32 v131, v122
	v_sub_f32_e32 v122, v132, v141
	v_exp_f32_e32 v132, v122
	ds_read2_b64 v[54:57], v185 offset1:2
	ds_read2_b64 v[58:61], v186 offset1:2
	ds_read2_b64 v[62:65], v187 offset1:2
	v_cvt_pk_bf16_f32 v122, v142, v143
	v_cvt_pk_bf16_f32 v123, v127, v128
	v_cvt_pk_bf16_f32 v124, v129, v130
	v_cvt_pk_bf16_f32 v125, v131, v132
	v_add_f32_e32 v142, 0, v142
	v_mov_b32_e32 v189, v141
	s_waitcnt lgkmcnt(2)
	v_mfma_f32_32x32x16_bf16 v[18:33], v[54:57], v[122:125], v[18:33]
	v_sub_f32_e32 v54, v133, v141
	s_waitcnt lgkmcnt(0)
	v_mfma_f32_32x32x16_bf16 v[34:49], v[62:65], v[122:125], v[34:49]
	v_exp_f32_e32 v63, v54
	v_sub_f32_e32 v54, v134, v141
	v_exp_f32_e32 v64, v54
	v_sub_f32_e32 v54, v135, v141
	v_exp_f32_e32 v65, v54
	v_sub_f32_e32 v54, v136, v141
	v_exp_f32_e32 v122, v54
	v_sub_f32_e32 v54, v137, v141
	v_add_f32_e32 v62, v143, v142
	v_exp_f32_e32 v123, v54
	v_sub_f32_e32 v54, v138, v141
	v_add_f32_e32 v62, v127, v62
	v_exp_f32_e32 v124, v54
	v_sub_f32_e32 v54, v139, v141
	v_add_f32_e32 v62, v128, v62
	v_exp_f32_e32 v125, v54
	v_sub_f32_e32 v54, v140, v141
	v_add_f32_e32 v62, v129, v62
	v_exp_f32_e32 v127, v54
	v_add_f32_e32 v62, v130, v62
	v_add_f32_e32 v62, v131, v62
	v_add_f32_e32 v62, v132, v62
	v_cvt_pk_bf16_f32 v54, v63, v64
	v_cvt_pk_bf16_f32 v55, v65, v122
	v_cvt_pk_bf16_f32 v56, v123, v124
	v_cvt_pk_bf16_f32 v57, v125, v127
	v_add_f32_e32 v62, v63, v62
	s_nop 0
	v_mfma_f32_32x32x16_bf16 v[34:49], v[58:61], v[54:57], v[34:49]
	v_add_f32_e32 v58, v64, v62
	v_add_f32_e32 v58, v65, v58
	v_add_f32_e32 v58, v122, v58
	v_add_f32_e32 v58, v123, v58
	v_add_f32_e32 v58, v124, v58
	v_add_f32_e32 v58, v125, v58
	v_add_f32_e32 v58, v127, v58
	v_mfma_f32_32x32x16_bf16 v[18:33], v[50:53], v[54:57], v[18:33]
	v_fmac_f32_e32 v58, v146, v126
	v_mov_b32_e32 v146, v58
